# v62 + P5 first peeled tile: wait only for the older B loads (vmcnt(10)), not for the five A-tile DMAs issued just before
# speedup vs baseline: 1.0123x; 1.0009x over previous
.LBB0_648:
	s_mov_b32 m0, s85
	ds_read_b64_tr_b16 v[198:199], v187
	ds_read_b64_tr_b16 v[180:181], v187 offset:32
	ds_read_b64_tr_b16 v[202:203], v187 offset:64
	ds_read_b64_tr_b16 v[176:177], v187 offset:96
	ds_read_b64_tr_b16 v[200:201], v188
	ds_read_b64_tr_b16 v[182:183], v188 offset:32
	ds_read_b64_tr_b16 v[204:205], v188 offset:64
	ds_read_b64_tr_b16 v[178:179], v188 offset:96
	ds_read_b128 v[206:209], v186
	ds_read_b128 v[210:213], v186 offset:2048
	ds_read_b128 v[214:217], v186 offset:4096
	buffer_load_dwordx4 v189, s[20:23], s49 offen lds
	s_mov_b32 m0, s7
	s_add_i32 s16, s65, -1
	buffer_load_dwordx4 v192, s[20:23], s49 offen lds
	s_mov_b32 m0, s6
	s_and_b32 s25, s67, 0xffff
	buffer_load_dwordx4 v191, s[20:23], s49 offen lds
	s_mov_b32 m0, s47
	s_mov_b32 s24, s66
	buffer_load_dwordx4 v190, s[20:23], s49 offen lds
	s_mov_b32 m0, s48
	s_mov_b32 s26, s18
	buffer_load_dwordx4 v193, s[20:23], s49 offen lds
	v_mbcnt_lo_u32_b32 v189, -1, 0
	v_mbcnt_hi_u32_b32 v189, -1, v189
	s_mov_b32 s27, s19
	v_ashrrev_i32_e32 v190, 2, v189
	v_add_u32_e32 v190, s78, v190
	v_add_u32_e32 v191, s81, v190
	v_min_i32_e32 v192, s16, v191
	v_add_u32_e32 v193, 64, v191
	v_add_u32_e32 v195, 0x80, v191
	v_add_u32_e32 v191, 0xc0, v191
	v_add_u32_e32 v190, s82, v190
	v_min_i32_e32 v193, s16, v193
	v_min_i32_e32 v195, s16, v195
	v_min_i32_e32 v191, s16, v191
	v_min_i32_e32 v190, s16, v190
	v_lshlrev_b32_e32 v192, 2, v192
	v_lshlrev_b32_e32 v193, 2, v193
	v_lshlrev_b32_e32 v195, 2, v195
	v_lshlrev_b32_e32 v191, 2, v191
	v_lshlrev_b32_e32 v190, 2, v190
	buffer_load_dword v192, v192, s[24:27], 0 offen
	s_nop 0
	buffer_load_dword v193, v193, s[24:27], 0 offen
	s_nop 0
	buffer_load_dword v195, v195, s[24:27], 0 offen
	s_nop 0
	buffer_load_dword v191, v191, s[24:27], 0 offen
	s_nop 0
	buffer_load_dword v190, v190, s[24:27], 0 offen
	v_lshlrev_b32_e32 v197, 4, v189
	v_and_b32_e32 v189, 32, v189
	v_and_b32_e32 v197, 48, v197
	v_bitop3_b32 v197, v197, s84, v189 bitop3:0xde
	s_and_b32 s25, s77, 0xffff
	s_mov_b32 s24, s55
	s_and_b32 s29, s80, 0xffff
	s_mov_b32 s28, s79
	s_mov_b32 s16, s55
	s_mov_b32 s36, s79
	s_mov_b32 s38, s18
	s_mov_b32 s39, s19
	s_waitcnt lgkmcnt(2)
	v_mfma_f32_16x16x32_bf16 v[172:175], v[198:201], v[206:209], v[172:175]
	s_mov_b32 s17, s25
	s_mov_b32 s37, s29
	s_waitcnt vmcnt(10)
	v_mfma_f32_16x16x32_bf16 v[168:171], v[180:183], v[206:209], v[168:171]
	v_mfma_f32_16x16x32_bf16 v[164:167], v[202:205], v[206:209], v[164:167]
	v_mfma_f32_16x16x32_bf16 v[160:163], v[176:179], v[206:209], v[160:163]
	ds_read_b128 v[206:209], v186 offset:6144
	v_cvt_pk_bf16_f32 v15, v14, v15
	v_cvt_pk_bf16_f32 v14, v12, v13
	s_waitcnt lgkmcnt(2)
	v_mfma_f32_16x16x32_bf16 v[156:159], v[198:201], v[210:213], v[156:159]
	ds_write_b64 v185, v[14:15] offset:34816
	v_mfma_f32_16x16x32_bf16 v[152:155], v[180:183], v[210:213], v[152:155]
	v_mfma_f32_16x16x32_bf16 v[148:151], v[202:205], v[210:213], v[148:151]
	v_mfma_f32_16x16x32_bf16 v[144:147], v[176:179], v[210:213], v[144:147]
	buffer_load_dwordx4 v[12:15], v184, s[16:19], 0 offen
	ds_read_b128 v[210:213], v186 offset:8192
	s_waitcnt lgkmcnt(3)
	v_mfma_f32_16x16x32_bf16 v[132:135], v[198:201], v[214:217], v[132:135]
	v_mfma_f32_16x16x32_bf16 v[124:127], v[180:183], v[214:217], v[124:127]
	v_mfma_f32_16x16x32_bf16 v[120:123], v[202:205], v[214:217], v[120:123]
	v_mfma_f32_16x16x32_bf16 v[140:143], v[176:179], v[214:217], v[140:143]
	ds_read_b128 v[214:217], v186 offset:10240
	v_cvt_pk_bf16_f32 v3, v2, v3
	v_cvt_pk_bf16_f32 v2, v0, v1
	s_waitcnt lgkmcnt(3)
	v_mfma_f32_16x16x32_bf16 v[136:139], v[198:201], v[206:209], v[136:139]
	ds_write_b64 v185, v[2:3] offset:43520
	v_mfma_f32_16x16x32_bf16 v[128:131], v[180:183], v[206:209], v[128:131]
	v_mfma_f32_16x16x32_bf16 v[116:119], v[202:205], v[206:209], v[116:119]
	v_mfma_f32_16x16x32_bf16 v[112:115], v[176:179], v[206:209], v[112:115]
	buffer_load_dwordx4 v[0:3], v184, s[16:19], s19 offen
	ds_read_b128 v[206:209], v186 offset:12288
	s_waitcnt lgkmcnt(3)
	v_mfma_f32_16x16x32_bf16 v[100:103], v[198:201], v[210:213], v[100:103]
	v_mfma_f32_16x16x32_bf16 v[92:95], v[180:183], v[210:213], v[92:95]
	v_mfma_f32_16x16x32_bf16 v[88:91], v[202:205], v[210:213], v[88:91]
	v_mfma_f32_16x16x32_bf16 v[108:111], v[176:179], v[210:213], v[108:111]
	ds_read_b128 v[210:213], v186 offset:14336
	v_cvt_pk_bf16_f32 v31, v30, v31
	v_cvt_pk_bf16_f32 v30, v28, v29
	s_waitcnt lgkmcnt(3)
	v_mfma_f32_16x16x32_bf16 v[104:107], v[198:201], v[214:217], v[104:107]
	ds_write_b64 v185, v[30:31] offset:52224
	v_mfma_f32_16x16x32_bf16 v[96:99], v[180:183], v[214:217], v[96:99]
	v_mfma_f32_16x16x32_bf16 v[84:87], v[202:205], v[214:217], v[84:87]
	v_mfma_f32_16x16x32_bf16 v[80:83], v[176:179], v[214:217], v[80:83]
	buffer_load_dwordx4 v[28:31], v184, s[16:19], s87 offen
	ds_read_b128 v[214:217], v186 offset:16384
	s_waitcnt lgkmcnt(3)
	v_mfma_f32_16x16x32_bf16 v[72:75], v[198:201], v[206:209], v[72:75]
	v_mfma_f32_16x16x32_bf16 v[64:67], v[180:183], v[206:209], v[64:67]
	v_mfma_f32_16x16x32_bf16 v[60:63], v[202:205], v[206:209], v[60:63]
	v_mfma_f32_16x16x32_bf16 v[76:79], v[176:179], v[206:209], v[76:79]
	ds_read_b128 v[206:209], v186 offset:1024
	v_cvt_pk_bf16_f32 v27, v26, v27
	v_cvt_pk_bf16_f32 v26, v24, v25
	s_waitcnt lgkmcnt(3)
	v_mfma_f32_16x16x32_bf16 v[68:71], v[198:201], v[210:213], v[68:71]
	ds_write_b64 v185, v[26:27] offset:60928
	v_mfma_f32_16x16x32_bf16 v[56:59], v[180:183], v[210:213], v[56:59]
	v_mfma_f32_16x16x32_bf16 v[52:55], v[202:205], v[210:213], v[52:55]
	v_mfma_f32_16x16x32_bf16 v[48:51], v[176:179], v[210:213], v[48:51]
	buffer_load_dwordx4 v[24:27], v184, s[16:19], s88 offen
	ds_read_b128 v[210:213], v186 offset:3072
	s_waitcnt lgkmcnt(3)
	v_mfma_f32_16x16x32_bf16 v[44:47], v[198:201], v[214:217], v[44:47]
	ds_read_b64_tr_b16 v[200:201], v188 offset:17408
	ds_read_b64_tr_b16 v[220:221], v188 offset:17440
	ds_read_b64_tr_b16 v[198:199], v187 offset:17408
	ds_read_b64_tr_b16 v[218:219], v187 offset:17440
	v_mfma_f32_16x16x32_bf16 v[40:43], v[180:183], v[214:217], v[40:43]
	ds_read_b64_tr_b16 v[180:181], v187 offset:17472
	ds_read_b64_tr_b16 v[182:183], v188 offset:17472
	v_mfma_f32_16x16x32_bf16 v[32:35], v[176:179], v[214:217], v[32:35]
	ds_read_b64_tr_b16 v[176:177], v187 offset:17504
	ds_read_b64_tr_b16 v[178:179], v188 offset:17504
	v_mfma_f32_16x16x32_bf16 v[36:39], v[202:205], v[214:217], v[36:39]
	ds_read_b128 v[202:205], v186 offset:5120
	v_cvt_pk_bf16_f32 v23, v22, v23
	v_cvt_pk_bf16_f32 v22, v20, v21
	s_waitcnt lgkmcnt(6)
	v_mfma_f32_16x16x32_bf16 v[172:175], v[198:201], v[206:209], v[172:175]
	ds_write_b64 v185, v[22:23] offset:34880
	s_waitcnt lgkmcnt(6)
	v_mfma_f32_16x16x32_bf16 v[168:171], v[218:221], v[206:209], v[168:171]
	s_waitcnt lgkmcnt(4)
	v_mfma_f32_16x16x32_bf16 v[164:167], v[180:183], v[206:209], v[164:167]
	s_waitcnt lgkmcnt(2)
	v_mfma_f32_16x16x32_bf16 v[160:163], v[176:179], v[206:209], v[160:163]
	buffer_load_dwordx4 v[20:23], v184, s[36:39], 0 offen
	ds_read_b128 v[206:209], v186 offset:7168
	v_mfma_f32_16x16x32_bf16 v[156:159], v[198:201], v[210:213], v[156:159]
	v_mfma_f32_16x16x32_bf16 v[152:155], v[218:221], v[210:213], v[152:155]
	v_mfma_f32_16x16x32_bf16 v[148:151], v[180:183], v[210:213], v[148:151]
	v_mfma_f32_16x16x32_bf16 v[144:147], v[176:179], v[210:213], v[144:147]
	ds_read_b128 v[210:213], v186 offset:9216
	v_cvt_pk_bf16_f32 v7, v6, v7
	v_cvt_pk_bf16_f32 v6, v4, v5
	s_waitcnt lgkmcnt(3)
	v_mfma_f32_16x16x32_bf16 v[132:135], v[198:201], v[202:205], v[132:135]
	ds_write_b64 v185, v[6:7] offset:43584
	v_mfma_f32_16x16x32_bf16 v[124:127], v[218:221], v[202:205], v[124:127]
	v_mfma_f32_16x16x32_bf16 v[120:123], v[180:183], v[202:205], v[120:123]
	v_mfma_f32_16x16x32_bf16 v[140:143], v[176:179], v[202:205], v[140:143]
	buffer_load_dwordx4 v[4:7], v184, s[36:39], s19 offen
	ds_read_b128 v[202:205], v186 offset:11264
	s_waitcnt lgkmcnt(3)
	v_mfma_f32_16x16x32_bf16 v[136:139], v[198:201], v[206:209], v[136:139]
	v_mfma_f32_16x16x32_bf16 v[128:131], v[218:221], v[206:209], v[128:131]
	v_mfma_f32_16x16x32_bf16 v[116:119], v[180:183], v[206:209], v[116:119]
	v_mfma_f32_16x16x32_bf16 v[112:115], v[176:179], v[206:209], v[112:115]
	ds_read_b128 v[206:209], v186 offset:13312
	v_cvt_pk_bf16_f32 v11, v10, v11
	v_cvt_pk_bf16_f32 v10, v8, v9
	s_waitcnt lgkmcnt(3)
	v_mfma_f32_16x16x32_bf16 v[100:103], v[198:201], v[210:213], v[100:103]
	ds_write_b64 v185, v[10:11] offset:52288
	v_mfma_f32_16x16x32_bf16 v[92:95], v[218:221], v[210:213], v[92:95]
	v_mfma_f32_16x16x32_bf16 v[88:91], v[180:183], v[210:213], v[88:91]
	v_mfma_f32_16x16x32_bf16 v[108:111], v[176:179], v[210:213], v[108:111]
	buffer_load_dwordx4 v[8:11], v184, s[36:39], s87 offen
	ds_read_b128 v[210:213], v186 offset:15360
	s_waitcnt lgkmcnt(3)
	v_mfma_f32_16x16x32_bf16 v[104:107], v[198:201], v[202:205], v[104:107]
	v_mfma_f32_16x16x32_bf16 v[96:99], v[218:221], v[202:205], v[96:99]
	v_mfma_f32_16x16x32_bf16 v[84:87], v[180:183], v[202:205], v[84:87]
	v_mfma_f32_16x16x32_bf16 v[80:83], v[176:179], v[202:205], v[80:83]
	ds_read_b128 v[202:205], v186 offset:17408
	v_cvt_pk_bf16_f32 v19, v18, v19
	v_cvt_pk_bf16_f32 v18, v16, v17
	s_waitcnt lgkmcnt(3)
	v_mfma_f32_16x16x32_bf16 v[72:75], v[198:201], v[206:209], v[72:75]
	ds_write_b64 v185, v[18:19] offset:60992
	v_mfma_f32_16x16x32_bf16 v[64:67], v[218:221], v[206:209], v[64:67]
	v_mfma_f32_16x16x32_bf16 v[60:63], v[180:183], v[206:209], v[60:63]
	v_mfma_f32_16x16x32_bf16 v[76:79], v[176:179], v[206:209], v[76:79]
	buffer_load_dwordx4 v[16:19], v184, s[36:39], s88 offen
	s_waitcnt lgkmcnt(2)
	v_mfma_f32_16x16x32_bf16 v[68:71], v[198:201], v[210:213], v[68:71]
	v_mfma_f32_16x16x32_bf16 v[56:59], v[218:221], v[210:213], v[56:59]
	v_mfma_f32_16x16x32_bf16 v[52:55], v[180:183], v[210:213], v[52:55]
	v_mfma_f32_16x16x32_bf16 v[48:51], v[176:179], v[210:213], v[48:51]
	s_waitcnt lgkmcnt(1)
	v_mfma_f32_16x16x32_bf16 v[44:47], v[198:201], v[202:205], v[44:47]
	v_mfma_f32_16x16x32_bf16 v[40:43], v[218:221], v[202:205], v[40:43]
	v_mfma_f32_16x16x32_bf16 v[36:39], v[180:183], v[202:205], v[36:39]
	v_mfma_f32_16x16x32_bf16 v[32:35], v[176:179], v[202:205], v[32:35]
	s_waitcnt vmcnt(8)
	v_lshlrev_b32_e32 v189, 10, v192
	v_lshlrev_b32_e32 v192, 10, v193
	v_lshlrev_b32_e32 v193, 10, v195
	v_lshlrev_b32_e32 v195, 10, v191
	v_lshlrev_b32_e32 v243, 10, v190
	v_and_or_b32 v189, v189, s83, v197
	v_and_or_b32 v192, v192, s83, v197
	v_and_or_b32 v191, v193, s83, v197
	v_and_or_b32 v190, v195, s83, v197
	v_and_or_b32 v193, v243, s83, v197
	s_mov_b32 m0, s46
	s_waitcnt lgkmcnt(0)
	s_barrier
	v_mbcnt_lo_u32_b32 v244, -1, 0
	v_mbcnt_hi_u32_b32 v244, -1, v244
	s_add_i32 s100, s54, s4
	v_ashrrev_i32_e32 v238, 1, v244
	v_and_b32_e32 v238, -8, v238
	v_add_u32_e32 v244, s100, v238
	v_ashrrev_i32_e32 v245, 31, v244
	v_lshlrev_b64 v[238:239], 2, v[244:245]
	v_lshl_add_u64 v[240:241], s[56:57], 0, v[238:239]
	v_lshl_add_u64 v[238:239], s[58:59], 0, v[238:239]
	global_load_dwordx4 v[252:255], v[240:241], off
	global_load_dwordx4 v[248:251], v[238:239], off
	global_load_dwordx4 v[244:247], v[240:241], off offset:16
	s_nop 0
	global_load_dwordx4 v[238:241], v[238:239], off offset:16
	ds_read_b64_tr_b16 v[178:179], v188 offset:34816
	ds_read_b64_tr_b16 v[176:177], v187 offset:34816
	ds_read_b64_tr_b16 v[180:181], v187 offset:34848
	ds_read_b64_tr_b16 v[198:199], v187 offset:34880
	ds_read_b64_tr_b16 v[202:203], v187 offset:34912
	ds_read_b128 v[206:209], v186 offset:36864
	ds_read_b64_tr_b16 v[182:183], v188 offset:34848
	ds_read_b64_tr_b16 v[200:201], v188 offset:34880
	ds_read_b64_tr_b16 v[204:205], v188 offset:34912
	ds_read_b128 v[210:213], v186 offset:38912
	ds_read_b128 v[214:217], v186 offset:40960
	buffer_load_dwordx4 v189, s[20:23], 0 offen lds
	s_mov_b32 m0, s86
	s_waitcnt lgkmcnt(5)
	v_mfma_f32_16x16x32_bf16 v[172:175], v[176:179], v[206:209], v[172:175]
	buffer_load_dwordx4 v192, s[20:23], 0 offen lds
	s_mov_b32 m0, s89
	s_nop 0
	buffer_load_dwordx4 v191, s[20:23], 0 offen lds
	s_mov_b32 m0, s90
	s_waitcnt lgkmcnt(4)
	v_mfma_f32_16x16x32_bf16 v[168:171], v[180:183], v[206:209], v[168:171]
	buffer_load_dwordx4 v190, s[20:23], 0 offen lds
	s_mov_b32 m0, s91
	s_nop 0
	buffer_load_dwordx4 v193, s[20:23], 0 offen lds
	s_waitcnt lgkmcnt(3)
	v_mfma_f32_16x16x32_bf16 v[164:167], v[198:201], v[206:209], v[164:167]
	s_waitcnt lgkmcnt(2)
	v_mfma_f32_16x16x32_bf16 v[160:163], v[202:205], v[206:209], v[160:163]
	ds_read_b128 v[206:209], v186 offset:43008
	s_waitcnt vmcnt(16)
	v_cvt_pk_bf16_f32 v15, v14, v15
	v_cvt_pk_bf16_f32 v14, v12, v13
	s_waitcnt lgkmcnt(2)
	v_mfma_f32_16x16x32_bf16 v[156:159], v[176:179], v[210:213], v[156:159]
	ds_write_b64 v185, v[14:15]
	v_mfma_f32_16x16x32_bf16 v[152:155], v[180:183], v[210:213], v[152:155]
	v_mfma_f32_16x16x32_bf16 v[148:151], v[198:201], v[210:213], v[148:151]
	v_mfma_f32_16x16x32_bf16 v[144:147], v[202:205], v[210:213], v[144:147]
	buffer_load_dwordx4 v[12:15], v184, s[16:19], s93 offen
	ds_read_b128 v[210:213], v186 offset:45056
	s_waitcnt lgkmcnt(3)
	v_mfma_f32_16x16x32_bf16 v[132:135], v[176:179], v[214:217], v[132:135]
	v_mfma_f32_16x16x32_bf16 v[124:127], v[180:183], v[214:217], v[124:127]
	v_mfma_f32_16x16x32_bf16 v[120:123], v[198:201], v[214:217], v[120:123]
	v_mfma_f32_16x16x32_bf16 v[140:143], v[202:205], v[214:217], v[140:143]
	ds_read_b128 v[214:217], v186 offset:47104
	s_waitcnt vmcnt(16)
	v_cvt_pk_bf16_f32 v3, v2, v3
	v_cvt_pk_bf16_f32 v2, v0, v1
	s_waitcnt lgkmcnt(3)
	v_mfma_f32_16x16x32_bf16 v[136:139], v[176:179], v[206:209], v[136:139]
	ds_write_b64 v185, v[2:3] offset:8704
	v_mfma_f32_16x16x32_bf16 v[128:131], v[180:183], v[206:209], v[128:131]
	v_mfma_f32_16x16x32_bf16 v[116:119], v[198:201], v[206:209], v[116:119]
	v_mfma_f32_16x16x32_bf16 v[112:115], v[202:205], v[206:209], v[112:115]
	buffer_load_dwordx4 v[0:3], v184, s[16:19], s94 offen
	ds_read_b128 v[206:209], v186 offset:49152
	s_waitcnt lgkmcnt(3)
	v_mfma_f32_16x16x32_bf16 v[100:103], v[176:179], v[210:213], v[100:103]
	v_mfma_f32_16x16x32_bf16 v[92:95], v[180:183], v[210:213], v[92:95]
	v_mfma_f32_16x16x32_bf16 v[88:91], v[198:201], v[210:213], v[88:91]
	v_mfma_f32_16x16x32_bf16 v[108:111], v[202:205], v[210:213], v[108:111]
	ds_read_b128 v[210:213], v186 offset:51200
	s_waitcnt vmcnt(16)
	v_cvt_pk_bf16_f32 v31, v30, v31
	v_cvt_pk_bf16_f32 v30, v28, v29
	s_waitcnt lgkmcnt(3)
	v_mfma_f32_16x16x32_bf16 v[104:107], v[176:179], v[214:217], v[104:107]
	ds_write_b64 v185, v[30:31] offset:17408
	v_mfma_f32_16x16x32_bf16 v[96:99], v[180:183], v[214:217], v[96:99]
	v_mfma_f32_16x16x32_bf16 v[84:87], v[198:201], v[214:217], v[84:87]
	v_mfma_f32_16x16x32_bf16 v[80:83], v[202:205], v[214:217], v[80:83]
	buffer_load_dwordx4 v[28:31], v184, s[16:19], s95 offen
	ds_read_b128 v[214:217], v186 offset:53248
	s_waitcnt lgkmcnt(3)
	v_mfma_f32_16x16x32_bf16 v[72:75], v[176:179], v[206:209], v[72:75]
	v_mfma_f32_16x16x32_bf16 v[64:67], v[180:183], v[206:209], v[64:67]
	v_mfma_f32_16x16x32_bf16 v[60:63], v[198:201], v[206:209], v[60:63]
	v_mfma_f32_16x16x32_bf16 v[76:79], v[202:205], v[206:209], v[76:79]
	ds_read_b128 v[206:209], v186 offset:37888
	s_waitcnt vmcnt(16)
	v_cvt_pk_bf16_f32 v27, v26, v27
	v_cvt_pk_bf16_f32 v26, v24, v25
	s_waitcnt lgkmcnt(3)
	v_mfma_f32_16x16x32_bf16 v[68:71], v[176:179], v[210:213], v[68:71]
	ds_write_b64 v185, v[26:27] offset:26112
	v_mfma_f32_16x16x32_bf16 v[56:59], v[180:183], v[210:213], v[56:59]
	v_mfma_f32_16x16x32_bf16 v[52:55], v[198:201], v[210:213], v[52:55]
	v_mfma_f32_16x16x32_bf16 v[48:51], v[202:205], v[210:213], v[48:51]
	buffer_load_dwordx4 v[24:27], v184, s[16:19], s96 offen
	ds_read_b128 v[210:213], v186 offset:39936
	s_waitcnt lgkmcnt(3)
	v_mfma_f32_16x16x32_bf16 v[44:47], v[176:179], v[214:217], v[44:47]
	ds_read_b64_tr_b16 v[178:179], v188 offset:52224
	ds_read_b64_tr_b16 v[220:221], v188 offset:52256
	ds_read_b64_tr_b16 v[176:177], v187 offset:52224
	ds_read_b64_tr_b16 v[218:219], v187 offset:52256
	v_mfma_f32_16x16x32_bf16 v[40:43], v[180:183], v[214:217], v[40:43]
	v_mfma_f32_16x16x32_bf16 v[180:183], v[198:201], v[214:217], v[36:39]
	ds_read_b64_tr_b16 v[198:199], v187 offset:52288
	ds_read_b64_tr_b16 v[200:201], v188 offset:52288
	v_mfma_f32_16x16x32_bf16 v[32:35], v[202:205], v[214:217], v[32:35]
	ds_read_b64_tr_b16 v[202:203], v187 offset:52320
	ds_read_b64_tr_b16 v[204:205], v188 offset:52320
	ds_read_b128 v[36:39], v186 offset:41984
	s_waitcnt vmcnt(16)
	v_cvt_pk_bf16_f32 v23, v22, v23
	v_cvt_pk_bf16_f32 v22, v20, v21
	s_waitcnt lgkmcnt(6)
	v_mfma_f32_16x16x32_bf16 v[214:217], v[176:179], v[206:209], v[172:175]
	ds_write_b64 v185, v[22:23] offset:64
	s_waitcnt lgkmcnt(6)
	v_mfma_f32_16x16x32_bf16 v[222:225], v[218:221], v[206:209], v[168:171]
	s_waitcnt lgkmcnt(4)
	v_mfma_f32_16x16x32_bf16 v[226:229], v[198:201], v[206:209], v[164:167]
	s_waitcnt lgkmcnt(2)
	v_mfma_f32_16x16x32_bf16 v[206:209], v[202:205], v[206:209], v[160:163]
	buffer_load_dwordx4 v[20:23], v184, s[36:39], s93 offen
	ds_read_b128 v[230:233], v186 offset:44032
	v_mfma_f32_16x16x32_bf16 v[172:175], v[176:179], v[210:213], v[156:159]
	v_mfma_f32_16x16x32_bf16 v[164:167], v[218:221], v[210:213], v[152:155]
	v_mfma_f32_16x16x32_bf16 v[168:171], v[198:201], v[210:213], v[148:151]
	v_mfma_f32_16x16x32_bf16 v[160:163], v[202:205], v[210:213], v[144:147]
	ds_read_b128 v[210:213], v186 offset:46080
	s_waitcnt vmcnt(16)
	v_cvt_pk_bf16_f32 v7, v6, v7
	v_cvt_pk_bf16_f32 v6, v4, v5
	s_waitcnt lgkmcnt(3)
	v_mfma_f32_16x16x32_bf16 v[156:159], v[176:179], v[36:39], v[132:135]
	ds_write_b64 v185, v[6:7] offset:8768
	v_mfma_f32_16x16x32_bf16 v[144:147], v[218:221], v[36:39], v[124:127]
	v_mfma_f32_16x16x32_bf16 v[152:155], v[198:201], v[36:39], v[120:123]
	v_mfma_f32_16x16x32_bf16 v[148:151], v[202:205], v[36:39], v[140:143]
	buffer_load_dwordx4 v[4:7], v184, s[36:39], s94 offen
	ds_read_b128 v[36:39], v186 offset:48128
	s_waitcnt lgkmcnt(3)
	v_mfma_f32_16x16x32_bf16 v[140:143], v[176:179], v[230:233], v[136:139]
	v_mfma_f32_16x16x32_bf16 v[132:135], v[218:221], v[230:233], v[128:131]
	v_mfma_f32_16x16x32_bf16 v[136:139], v[198:201], v[230:233], v[116:119]
	v_mfma_f32_16x16x32_bf16 v[128:131], v[202:205], v[230:233], v[112:115]
	ds_read_b128 v[230:233], v186 offset:50176
	s_waitcnt vmcnt(16)
	v_cvt_pk_bf16_f32 v11, v10, v11
	v_cvt_pk_bf16_f32 v10, v8, v9
	s_waitcnt lgkmcnt(3)
	v_mfma_f32_16x16x32_bf16 v[124:127], v[176:179], v[210:213], v[100:103]
	ds_write_b64 v185, v[10:11] offset:17472
	v_mfma_f32_16x16x32_bf16 v[112:115], v[218:221], v[210:213], v[92:95]
	v_mfma_f32_16x16x32_bf16 v[120:123], v[198:201], v[210:213], v[88:91]
	v_mfma_f32_16x16x32_bf16 v[116:119], v[202:205], v[210:213], v[108:111]
	buffer_load_dwordx4 v[8:11], v184, s[36:39], s95 offen
	ds_read_b128 v[210:213], v186 offset:52224
	s_waitcnt lgkmcnt(3)
	v_mfma_f32_16x16x32_bf16 v[108:111], v[176:179], v[36:39], v[104:107]
	v_mfma_f32_16x16x32_bf16 v[100:103], v[218:221], v[36:39], v[96:99]
	v_mfma_f32_16x16x32_bf16 v[104:107], v[198:201], v[36:39], v[84:87]
	v_mfma_f32_16x16x32_bf16 v[96:99], v[202:205], v[36:39], v[80:83]
	ds_read_b128 v[234:237], v186 offset:54272
	s_waitcnt vmcnt(16)
	v_cvt_pk_bf16_f32 v19, v18, v19
	v_cvt_pk_bf16_f32 v18, v16, v17
	s_waitcnt lgkmcnt(3)
	v_mfma_f32_16x16x32_bf16 v[92:95], v[176:179], v[230:233], v[72:75]
	ds_write_b64 v185, v[18:19] offset:26176
	v_mfma_f32_16x16x32_bf16 v[80:83], v[218:221], v[230:233], v[64:67]
	v_mfma_f32_16x16x32_bf16 v[88:91], v[198:201], v[230:233], v[60:63]
	v_mfma_f32_16x16x32_bf16 v[84:87], v[202:205], v[230:233], v[76:79]
	buffer_load_dwordx4 v[16:19], v184, s[36:39], s96 offen
	s_waitcnt lgkmcnt(2)
	v_mfma_f32_16x16x32_bf16 v[76:79], v[176:179], v[210:213], v[68:71]
	v_mfma_f32_16x16x32_bf16 v[68:71], v[218:221], v[210:213], v[56:59]
	v_mfma_f32_16x16x32_bf16 v[72:75], v[198:201], v[210:213], v[52:55]
	v_mfma_f32_16x16x32_bf16 v[64:67], v[202:205], v[210:213], v[48:51]
	s_waitcnt lgkmcnt(1)
	v_mfma_f32_16x16x32_bf16 v[52:55], v[176:179], v[234:237], v[44:47]
	v_mfma_f32_16x16x32_bf16 v[36:39], v[218:221], v[234:237], v[40:43]
	v_mfma_f32_16x16x32_bf16 v[48:51], v[198:201], v[234:237], v[180:183]
	v_mfma_f32_16x16x32_bf16 v[32:35], v[202:205], v[234:237], v[32:35]
	s_waitcnt vmcnt(8)
	s_waitcnt lgkmcnt(0)
	s_barrier
	v_mbcnt_lo_u32_b32 v178, -1, 0
	v_mbcnt_hi_u32_b32 v178, -1, v178
	s_add_i32 s16, s54, s4
	v_ashrrev_i32_e32 v40, 1, v178
	v_and_b32_e32 v40, -8, v40
	v_add_u32_e32 v176, s16, v40
	v_ashrrev_i32_e32 v177, 31, v176
	v_lshlrev_b64 v[40:41], 2, v[176:177]
	v_lshl_add_u64 v[42:43], s[56:57], 0, v[40:41]
	v_lshl_add_u64 v[40:41], s[58:59], 0, v[40:41]
	s_nop 0
	s_mul_i32 s16, s72, 0x90
	v_and_or_b32 v178, v178, 15, s16
	v_add_u32_e32 v180, s68, v178
	v_ashrrev_i32_e32 v181, 31, v180
	v_lshlrev_b64 v[180:181], 12, v[180:181]
	v_lshl_add_u64 v[198:199], s[50:51], 0, v[180:181]
	v_lshlrev_b64 v[176:177], 1, v[176:177]
	v_lshl_add_u64 v[198:199], v[198:199], 0, v[176:177]
	s_add_i32 s16, s68, 0x50
	s_and_b64 vcc, exec, s[30:31]
	s_mov_b32 s54, s42
	s_mov_b64 s[58:59], s[62:63]
	s_mov_b64 s[56:57], s[60:61]
	s_mov_b64 s[30:31], s[18:19]
	s_mov_b64 s[26:27], s[18:19]
	v_add_f32_e32 v179, v214, v252
	v_add_f32_e32 v181, v226, v248
	v_add_f32_e32 v183, v215, v253
	v_add_f32_e32 v197, v216, v254
	v_add_f32_e32 v201, v228, v250
	v_add_f32_e32 v203, v217, v255
	v_add_f32_e32 v195, v227, v249
	v_add_f32_e32 v204, v229, v251
	v_add_f32_e32 v205, v222, v244
	v_add_f32_e32 v210, v223, v245
	v_add_f32_e32 v211, v224, v246
	s_waitcnt vmcnt(0)
	v_add_f32_e32 v212, v208, v240
	v_add_f32_e32 v213, v225, v247
	v_min_f32_e32 v180, 0x40e00000, v179
	v_med3_f32 v182, v181, s53, v194
	v_min_f32_e32 v181, 0x40e00000, v183
	v_min_f32_e32 v200, 0x40e00000, v197
	v_med3_f32 v202, v201, s53, v194
	v_min_f32_e32 v201, 0x40e00000, v203
	v_add_f32_e32 v214, v209, v241
	v_med3_f32 v183, v195, s53, v194
	v_med3_f32 v203, v204, s53, v194
	v_min_f32_e32 v204, 0x40e00000, v205
	v_min_f32_e32 v205, 0x40e00000, v210
	v_min_f32_e32 v208, 0x40e00000, v211
	v_med3_f32 v210, v212, s53, v194
	v_min_f32_e32 v209, 0x40e00000, v213
	v_mul_f32_e32 v179, 0x3fd9db23, v180
	v_mul_f32_e32 v195, 0x3fd9db23, v181
	v_mul_f32_e32 v197, 0x3fd9db23, v200
	v_mul_f32_e32 v212, 0x3fd9db23, v201
	v_med3_f32 v211, v214, s53, v194
	v_pk_add_f32 v[182:183], v[182:183], 1.0 op_sel_hi:[1,0]
	v_pk_add_f32 v[202:203], v[202:203], 1.0 op_sel_hi:[1,0]
	v_mul_f32_e32 v213, 0x3fd9db23, v204
	v_mul_f32_e32 v214, 0x3fd9db23, v205
	v_mul_f32_e32 v215, 0x3fd9db23, v208
	v_mul_f32_e32 v216, 0x3fd9db23, v209
	v_mul_f32_e32 v179, 0xbfb8aa3b, v179
	v_mul_f32_e32 v195, 0xbfb8aa3b, v195
	v_mul_f32_e32 v197, 0xbfb8aa3b, v197
	v_mul_f32_e32 v212, 0xbfb8aa3b, v212
	v_pk_mul_f32 v[200:201], v[200:201], v[202:203]
	v_pk_mul_f32 v[180:181], v[180:181], v[182:183]
	v_mul_f32_e32 v182, 0xbfb8aa3b, v213
	v_mul_f32_e32 v183, 0xbfb8aa3b, v214
	v_mul_f32_e32 v202, 0xbfb8aa3b, v215
	v_mul_f32_e32 v203, 0xbfb8aa3b, v216
	v_exp_f32_e32 v179, v179
	v_exp_f32_e32 v195, v195
	v_exp_f32_e32 v197, v197
	v_exp_f32_e32 v212, v212
	v_exp_f32_e32 v182, v182
	v_exp_f32_e32 v183, v183
	v_exp_f32_e32 v202, v202
	v_exp_f32_e32 v203, v203
	v_add_f32_e32 v179, 1.0, v179
	v_add_f32_e32 v195, 1.0, v195
	v_add_f32_e32 v197, 1.0, v197
	v_add_f32_e32 v212, 1.0, v212
	v_add_f32_e32 v213, 1.0, v182
	v_add_f32_e32 v214, 1.0, v183
	v_add_f32_e32 v215, 1.0, v202
	v_add_f32_e32 v216, 1.0, v203
	v_rcp_f32_e32 v182, v179
	v_rcp_f32_e32 v183, v195
	v_rcp_f32_e32 v202, v197
	v_rcp_f32_e32 v203, v212
	v_add_f32_e32 v206, v206, v238
	v_add_f32_e32 v207, v207, v239
	v_rcp_f32_e32 v212, v213
	v_rcp_f32_e32 v213, v214
	v_rcp_f32_e32 v214, v215
	v_rcp_f32_e32 v215, v216
	v_med3_f32 v206, v206, s53, v194
	v_med3_f32 v207, v207, s53, v194
	v_pk_mul_f32 v[182:183], v[180:181], v[182:183]
	v_pk_mul_f32 v[180:181], v[200:201], v[202:203]
	v_pk_add_f32 v[206:207], v[206:207], 1.0 op_sel_hi:[1,0]
	v_cvt_pk_bf16_f32 v181, v180, v181
	v_cvt_pk_bf16_f32 v180, v182, v183
	v_pk_add_f32 v[182:183], v[210:211], 1.0 op_sel_hi:[1,0]
	v_pk_mul_f32 v[200:201], v[204:205], v[206:207]
	v_pk_mul_f32 v[182:183], v[208:209], v[182:183]
	v_add_f32_e32 v172, v172, v252
	v_pk_mul_f32 v[200:201], v[200:201], v[212:213]
	v_pk_mul_f32 v[182:183], v[182:183], v[214:215]
	v_min_f32_e32 v172, 0x40e00000, v172
	v_add_f32_e32 v173, v173, v253
	v_cvt_pk_bf16_f32 v183, v182, v183
	v_cvt_pk_bf16_f32 v182, v200, v201
	v_mul_f32_e32 v179, 0x3fd9db23, v172
	v_min_f32_e32 v173, 0x40e00000, v173
	global_store_dwordx4 v[198:199], v[180:183], off
	v_mul_f32_e32 v179, 0xbfb8aa3b, v179
	v_exp_f32_e32 v179, v179
	v_mul_f32_e32 v182, 0x3fd9db23, v173
	v_mul_f32_e32 v182, 0xbfb8aa3b, v182
	v_exp_f32_e32 v183, v182
	v_add_f32_e32 v174, v174, v254
	v_add_f32_e32 v179, 1.0, v179
	v_min_f32_e32 v174, 0x40e00000, v174
	v_rcp_f32_e32 v182, v179
	v_add_f32_e32 v179, 1.0, v183
	v_mul_f32_e32 v183, 0x3fd9db23, v174
	v_mul_f32_e32 v183, 0xbfb8aa3b, v183
	v_exp_f32_e32 v195, v183
	v_add_f32_e32 v175, v175, v255
	v_min_f32_e32 v175, 0x40e00000, v175
	v_rcp_f32_e32 v183, v179
	v_add_f32_e32 v179, 1.0, v195
	v_mul_f32_e32 v195, 0x3fd9db23, v175
	v_mul_f32_e32 v195, 0xbfb8aa3b, v195
	v_exp_f32_e32 v195, v195
	v_rcp_f32_e32 v198, v179
	v_add_f32_e32 v168, v168, v248
	v_add_f32_e32 v169, v169, v249
	v_add_f32_e32 v179, 1.0, v195
	v_add_f32_e32 v170, v170, v250
	v_add_f32_e32 v171, v171, v251
	v_rcp_f32_e32 v199, v179
	v_med3_f32 v168, v168, s53, v194
	v_med3_f32 v169, v169, s53, v194
	v_med3_f32 v170, v170, s53, v194
	v_med3_f32 v171, v171, s53, v194
	v_pk_add_f32 v[168:169], v[168:169], 1.0 op_sel_hi:[1,0]
	v_pk_add_f32 v[170:171], v[170:171], 1.0 op_sel_hi:[1,0]
	v_pk_mul_f32 v[168:169], v[172:173], v[168:169]
	v_pk_mul_f32 v[170:171], v[174:175], v[170:171]
	v_add_f32_e32 v164, v164, v244
	v_pk_mul_f32 v[172:173], v[168:169], v[182:183]
	v_pk_mul_f32 v[168:169], v[170:171], v[198:199]
	v_min_f32_e32 v164, 0x40e00000, v164
	v_cvt_pk_bf16_f32 v169, v168, v169
	v_mul_f32_e32 v168, 0x3fd9db23, v164
	v_add_f32_e32 v166, v166, v246
	v_add_f32_e32 v167, v167, v247
	v_mul_f32_e32 v168, 0xbfb8aa3b, v168
	v_add_f32_e32 v165, v165, v245
	v_min_f32_e32 v166, 0x40e00000, v166
	v_min_f32_e32 v167, 0x40e00000, v167
	v_exp_f32_e32 v170, v168
	v_cvt_pk_bf16_f32 v168, v172, v173
	v_min_f32_e32 v165, 0x40e00000, v165
	v_mul_f32_e32 v172, 0x3fd9db23, v166
	v_mul_f32_e32 v173, 0x3fd9db23, v167
	v_mul_f32_e32 v171, 0x3fd9db23, v165
	v_mul_f32_e32 v172, 0xbfb8aa3b, v172
	v_mul_f32_e32 v173, 0xbfb8aa3b, v173
	v_mul_f32_e32 v171, 0xbfb8aa3b, v171
	v_exp_f32_e32 v172, v172
	v_exp_f32_e32 v173, v173
	v_exp_f32_e32 v171, v171
	v_add_f32_e32 v170, 1.0, v170
	v_add_f32_e32 v172, 1.0, v172
	v_add_f32_e32 v173, 1.0, v173
	v_add_f32_e32 v171, 1.0, v171
	v_add_f32_e32 v162, v162, v240
	v_rcp_f32_e32 v172, v172
	v_add_f32_e32 v163, v163, v241
	v_rcp_f32_e32 v173, v173
	v_add_f32_e32 v160, v160, v238
	v_rcp_f32_e32 v170, v170
	v_add_f32_e32 v161, v161, v239
	v_rcp_f32_e32 v171, v171
	v_med3_f32 v162, v162, s53, v194
	v_med3_f32 v163, v163, s53, v194
	v_med3_f32 v160, v160, s53, v194
	v_med3_f32 v161, v161, s53, v194
	v_pk_add_f32 v[162:163], v[162:163], 1.0 op_sel_hi:[1,0]
	v_pk_add_f32 v[160:161], v[160:161], 1.0 op_sel_hi:[1,0]
	v_pk_mul_f32 v[162:163], v[166:167], v[162:163]
	v_add_f32_e32 v156, v156, v252
	v_add_f32_e32 v157, v157, v253
	v_add_f32_e32 v158, v158, v254
	v_add_f32_e32 v159, v159, v255
	v_pk_mul_f32 v[160:161], v[164:165], v[160:161]
	v_pk_mul_f32 v[162:163], v[162:163], v[172:173]
	v_min_f32_e32 v156, 0x40e00000, v156
	v_min_f32_e32 v157, 0x40e00000, v157
	v_min_f32_e32 v158, 0x40e00000, v158
	v_min_f32_e32 v159, 0x40e00000, v159
	v_pk_mul_f32 v[160:161], v[160:161], v[170:171]
	v_cvt_pk_bf16_f32 v171, v162, v163
	v_mul_f32_e32 v162, 0x3fd9db23, v156
	v_mul_f32_e32 v163, 0x3fd9db23, v157
	v_mul_f32_e32 v164, 0x3fd9db23, v158
	v_mul_f32_e32 v165, 0x3fd9db23, v159
	v_mul_f32_e32 v162, 0xbfb8aa3b, v162
	v_mul_f32_e32 v163, 0xbfb8aa3b, v163
	v_mul_f32_e32 v164, 0xbfb8aa3b, v164
	v_mul_f32_e32 v165, 0xbfb8aa3b, v165
	v_exp_f32_e32 v162, v162
	v_exp_f32_e32 v163, v163
	v_exp_f32_e32 v164, v164
	v_exp_f32_e32 v165, v165
	v_add_f32_e32 v162, 1.0, v162
	v_add_f32_e32 v163, 1.0, v163
	v_add_f32_e32 v164, 1.0, v164
	v_add_f32_e32 v165, 1.0, v165
	v_add_f32_e32 v152, v152, v248
	v_rcp_f32_e32 v162, v162
	v_add_f32_e32 v153, v153, v249
	v_rcp_f32_e32 v163, v163
	v_add_f32_e32 v154, v154, v250
	v_rcp_f32_e32 v164, v164
	v_add_f32_e32 v155, v155, v251
	v_rcp_f32_e32 v165, v165
	v_med3_f32 v152, v152, s53, v194
	v_med3_f32 v153, v153, s53, v194
	v_med3_f32 v154, v154, s53, v194
	v_med3_f32 v155, v155, s53, v194
	v_pk_add_f32 v[152:153], v[152:153], 1.0 op_sel_hi:[1,0]
	v_pk_add_f32 v[154:155], v[154:155], 1.0 op_sel_hi:[1,0]
	v_pk_mul_f32 v[152:153], v[156:157], v[152:153]
	v_pk_mul_f32 v[154:155], v[158:159], v[154:155]
	v_add_f32_e32 v144, v144, v244
	v_pk_mul_f32 v[156:157], v[152:153], v[162:163]
	v_pk_mul_f32 v[152:153], v[154:155], v[164:165]
	v_min_f32_e32 v144, 0x40e00000, v144
	v_cvt_pk_bf16_f32 v153, v152, v153
	v_mul_f32_e32 v152, 0x3fd9db23, v144
	v_add_f32_e32 v146, v146, v246
	v_add_f32_e32 v147, v147, v247
	v_mul_f32_e32 v152, 0xbfb8aa3b, v152
	v_add_f32_e32 v145, v145, v245
	v_min_f32_e32 v146, 0x40e00000, v146
	v_min_f32_e32 v147, 0x40e00000, v147
	v_exp_f32_e32 v154, v152
	v_cvt_pk_bf16_f32 v152, v156, v157
	v_min_f32_e32 v145, 0x40e00000, v145
	v_mul_f32_e32 v156, 0x3fd9db23, v146
	v_mul_f32_e32 v157, 0x3fd9db23, v147
	v_mul_f32_e32 v155, 0x3fd9db23, v145
	v_mul_f32_e32 v156, 0xbfb8aa3b, v156
	v_mul_f32_e32 v157, 0xbfb8aa3b, v157
	v_mul_f32_e32 v155, 0xbfb8aa3b, v155
	v_exp_f32_e32 v156, v156
	v_exp_f32_e32 v157, v157
	v_exp_f32_e32 v155, v155
	v_add_f32_e32 v154, 1.0, v154
	v_add_f32_e32 v156, 1.0, v156
	v_add_f32_e32 v157, 1.0, v157
	v_add_f32_e32 v155, 1.0, v155
	v_add_f32_e32 v150, v150, v240
	v_rcp_f32_e32 v156, v156
	v_add_f32_e32 v151, v151, v241
	v_rcp_f32_e32 v157, v157
	v_add_f32_e32 v148, v148, v238
	v_rcp_f32_e32 v154, v154
	v_add_f32_e32 v149, v149, v239
	v_rcp_f32_e32 v155, v155
	v_med3_f32 v150, v150, s53, v194
	v_med3_f32 v151, v151, s53, v194
	v_med3_f32 v148, v148, s53, v194
	v_med3_f32 v149, v149, s53, v194
	v_pk_add_f32 v[150:151], v[150:151], 1.0 op_sel_hi:[1,0]
	v_pk_add_f32 v[148:149], v[148:149], 1.0 op_sel_hi:[1,0]
	v_pk_mul_f32 v[146:147], v[146:147], v[150:151]
	v_add_f32_e32 v140, v140, v252
	v_add_f32_e32 v141, v141, v253
	v_add_f32_e32 v142, v142, v254
	v_add_f32_e32 v143, v143, v255
	v_pk_mul_f32 v[144:145], v[144:145], v[148:149]
	v_pk_mul_f32 v[146:147], v[146:147], v[156:157]
	v_min_f32_e32 v140, 0x40e00000, v140
	v_min_f32_e32 v141, 0x40e00000, v141
	v_min_f32_e32 v142, 0x40e00000, v142
	v_min_f32_e32 v143, 0x40e00000, v143
	v_pk_mul_f32 v[144:145], v[144:145], v[154:155]
	v_cvt_pk_bf16_f32 v155, v146, v147
	v_mul_f32_e32 v146, 0x3fd9db23, v140
	v_mul_f32_e32 v147, 0x3fd9db23, v141
	v_mul_f32_e32 v148, 0x3fd9db23, v142
	v_mul_f32_e32 v149, 0x3fd9db23, v143
	v_mul_f32_e32 v146, 0xbfb8aa3b, v146
	v_mul_f32_e32 v147, 0xbfb8aa3b, v147
	v_mul_f32_e32 v148, 0xbfb8aa3b, v148
	v_mul_f32_e32 v149, 0xbfb8aa3b, v149
	v_exp_f32_e32 v146, v146
	v_exp_f32_e32 v147, v147
	v_exp_f32_e32 v148, v148
	v_exp_f32_e32 v149, v149
	v_add_f32_e32 v146, 1.0, v146
	v_add_f32_e32 v147, 1.0, v147
	v_add_f32_e32 v148, 1.0, v148
	v_add_f32_e32 v149, 1.0, v149
	v_add_f32_e32 v136, v136, v248
	v_rcp_f32_e32 v146, v146
	v_add_f32_e32 v137, v137, v249
	v_rcp_f32_e32 v147, v147
	v_add_f32_e32 v138, v138, v250
	v_rcp_f32_e32 v148, v148
	v_add_f32_e32 v139, v139, v251
	v_rcp_f32_e32 v149, v149
	v_med3_f32 v136, v136, s53, v194
	v_med3_f32 v137, v137, s53, v194
	v_med3_f32 v138, v138, s53, v194
	v_med3_f32 v139, v139, s53, v194
	v_pk_add_f32 v[136:137], v[136:137], 1.0 op_sel_hi:[1,0]
	v_pk_add_f32 v[138:139], v[138:139], 1.0 op_sel_hi:[1,0]
	v_pk_mul_f32 v[136:137], v[140:141], v[136:137]
	v_pk_mul_f32 v[138:139], v[142:143], v[138:139]
	v_add_f32_e32 v132, v132, v244
	v_pk_mul_f32 v[140:141], v[136:137], v[146:147]
	v_pk_mul_f32 v[136:137], v[138:139], v[148:149]
	v_min_f32_e32 v132, 0x40e00000, v132
	v_cvt_pk_bf16_f32 v137, v136, v137
	v_mul_f32_e32 v136, 0x3fd9db23, v132
	v_add_f32_e32 v134, v134, v246
	v_add_f32_e32 v135, v135, v247
	v_mul_f32_e32 v136, 0xbfb8aa3b, v136
	v_add_f32_e32 v133, v133, v245
	v_min_f32_e32 v134, 0x40e00000, v134
	v_min_f32_e32 v135, 0x40e00000, v135
	v_exp_f32_e32 v138, v136
	v_cvt_pk_bf16_f32 v136, v140, v141
	v_min_f32_e32 v133, 0x40e00000, v133
	v_mul_f32_e32 v140, 0x3fd9db23, v134
	v_mul_f32_e32 v141, 0x3fd9db23, v135
	v_mul_f32_e32 v139, 0x3fd9db23, v133
	v_mul_f32_e32 v140, 0xbfb8aa3b, v140
	v_mul_f32_e32 v141, 0xbfb8aa3b, v141
	v_mul_f32_e32 v139, 0xbfb8aa3b, v139
	v_exp_f32_e32 v140, v140
	v_exp_f32_e32 v141, v141
	v_exp_f32_e32 v139, v139
	v_add_f32_e32 v138, 1.0, v138
	v_add_f32_e32 v140, 1.0, v140
	v_add_f32_e32 v141, 1.0, v141
	v_add_f32_e32 v139, 1.0, v139
	v_add_f32_e32 v130, v130, v240
	v_rcp_f32_e32 v140, v140
	v_add_f32_e32 v131, v131, v241
	v_rcp_f32_e32 v141, v141
	v_add_f32_e32 v128, v128, v238
	v_rcp_f32_e32 v138, v138
	v_add_f32_e32 v129, v129, v239
	v_rcp_f32_e32 v139, v139
	v_med3_f32 v130, v130, s53, v194
	v_med3_f32 v131, v131, s53, v194
	v_med3_f32 v128, v128, s53, v194
	v_med3_f32 v129, v129, s53, v194
	v_pk_add_f32 v[130:131], v[130:131], 1.0 op_sel_hi:[1,0]
	v_pk_add_f32 v[128:129], v[128:129], 1.0 op_sel_hi:[1,0]
	v_pk_mul_f32 v[130:131], v[134:135], v[130:131]
	v_add_f32_e32 v124, v124, v252
	v_add_f32_e32 v125, v125, v253
	v_add_f32_e32 v126, v126, v254
	v_add_f32_e32 v127, v127, v255
	v_pk_mul_f32 v[128:129], v[132:133], v[128:129]
	v_pk_mul_f32 v[130:131], v[130:131], v[140:141]
	v_min_f32_e32 v124, 0x40e00000, v124
	v_min_f32_e32 v125, 0x40e00000, v125
	v_min_f32_e32 v126, 0x40e00000, v126
	v_min_f32_e32 v127, 0x40e00000, v127
	v_pk_mul_f32 v[128:129], v[128:129], v[138:139]
	v_cvt_pk_bf16_f32 v139, v130, v131
	v_mul_f32_e32 v130, 0x3fd9db23, v124
	v_mul_f32_e32 v131, 0x3fd9db23, v125
	v_mul_f32_e32 v132, 0x3fd9db23, v126
	v_mul_f32_e32 v133, 0x3fd9db23, v127
	v_mul_f32_e32 v130, 0xbfb8aa3b, v130
	v_mul_f32_e32 v131, 0xbfb8aa3b, v131
	v_mul_f32_e32 v132, 0xbfb8aa3b, v132
	v_mul_f32_e32 v133, 0xbfb8aa3b, v133
	v_exp_f32_e32 v130, v130
	v_exp_f32_e32 v131, v131
	v_exp_f32_e32 v132, v132
	v_exp_f32_e32 v133, v133
	v_add_f32_e32 v130, 1.0, v130
	v_add_f32_e32 v131, 1.0, v131
	v_add_f32_e32 v132, 1.0, v132
	v_add_f32_e32 v133, 1.0, v133
	v_add_f32_e32 v120, v120, v248
	v_rcp_f32_e32 v130, v130
	v_add_f32_e32 v121, v121, v249
	v_rcp_f32_e32 v131, v131
	v_add_f32_e32 v122, v122, v250
	v_rcp_f32_e32 v132, v132
	v_add_f32_e32 v123, v123, v251
	v_rcp_f32_e32 v133, v133
	v_med3_f32 v120, v120, s53, v194
	v_med3_f32 v121, v121, s53, v194
	v_med3_f32 v122, v122, s53, v194
	v_med3_f32 v123, v123, s53, v194
	v_pk_add_f32 v[120:121], v[120:121], 1.0 op_sel_hi:[1,0]
	v_pk_add_f32 v[122:123], v[122:123], 1.0 op_sel_hi:[1,0]
	v_pk_mul_f32 v[120:121], v[124:125], v[120:121]
	v_pk_mul_f32 v[122:123], v[126:127], v[122:123]
	v_add_f32_e32 v112, v112, v244
	v_pk_mul_f32 v[124:125], v[120:121], v[130:131]
	v_pk_mul_f32 v[120:121], v[122:123], v[132:133]
	v_min_f32_e32 v112, 0x40e00000, v112
	v_cvt_pk_bf16_f32 v121, v120, v121
	v_mul_f32_e32 v120, 0x3fd9db23, v112
	v_add_f32_e32 v114, v114, v246
	v_add_f32_e32 v115, v115, v247
	v_mul_f32_e32 v120, 0xbfb8aa3b, v120
	v_add_f32_e32 v113, v113, v245
	v_min_f32_e32 v114, 0x40e00000, v114
	v_min_f32_e32 v115, 0x40e00000, v115
	v_exp_f32_e32 v122, v120
	v_cvt_pk_bf16_f32 v120, v124, v125
	v_min_f32_e32 v113, 0x40e00000, v113
	v_mul_f32_e32 v124, 0x3fd9db23, v114
	v_mul_f32_e32 v125, 0x3fd9db23, v115
	v_mul_f32_e32 v123, 0x3fd9db23, v113
	v_mul_f32_e32 v124, 0xbfb8aa3b, v124
	v_mul_f32_e32 v125, 0xbfb8aa3b, v125
	v_mul_f32_e32 v123, 0xbfb8aa3b, v123
	v_exp_f32_e32 v124, v124
	v_exp_f32_e32 v125, v125
	v_exp_f32_e32 v123, v123
	v_add_f32_e32 v122, 1.0, v122
	v_add_f32_e32 v124, 1.0, v124
	v_add_f32_e32 v125, 1.0, v125
	v_add_f32_e32 v123, 1.0, v123
	v_add_f32_e32 v118, v118, v240
	v_rcp_f32_e32 v124, v124
	v_add_f32_e32 v119, v119, v241
	v_rcp_f32_e32 v125, v125
	v_add_f32_e32 v116, v116, v238
	v_rcp_f32_e32 v122, v122
	v_add_f32_e32 v117, v117, v239
	v_rcp_f32_e32 v123, v123
	v_med3_f32 v118, v118, s53, v194
	v_med3_f32 v119, v119, s53, v194
	v_med3_f32 v116, v116, s53, v194
	v_med3_f32 v117, v117, s53, v194
	v_pk_add_f32 v[118:119], v[118:119], 1.0 op_sel_hi:[1,0]
	v_pk_add_f32 v[116:117], v[116:117], 1.0 op_sel_hi:[1,0]
	v_pk_mul_f32 v[114:115], v[114:115], v[118:119]
	v_add_f32_e32 v108, v108, v252
	v_add_f32_e32 v109, v109, v253
	v_add_f32_e32 v110, v110, v254
	v_add_f32_e32 v111, v111, v255
	v_pk_mul_f32 v[112:113], v[112:113], v[116:117]
	v_pk_mul_f32 v[114:115], v[114:115], v[124:125]
	v_min_f32_e32 v108, 0x40e00000, v108
	v_min_f32_e32 v109, 0x40e00000, v109
	v_min_f32_e32 v110, 0x40e00000, v110
	v_min_f32_e32 v111, 0x40e00000, v111
	v_pk_mul_f32 v[112:113], v[112:113], v[122:123]
	v_cvt_pk_bf16_f32 v123, v114, v115
	v_mul_f32_e32 v114, 0x3fd9db23, v108
	v_mul_f32_e32 v115, 0x3fd9db23, v109
	v_mul_f32_e32 v116, 0x3fd9db23, v110
	v_mul_f32_e32 v117, 0x3fd9db23, v111
	v_mul_f32_e32 v114, 0xbfb8aa3b, v114
	v_mul_f32_e32 v115, 0xbfb8aa3b, v115
	v_mul_f32_e32 v116, 0xbfb8aa3b, v116
	v_mul_f32_e32 v117, 0xbfb8aa3b, v117
	v_exp_f32_e32 v114, v114
	v_exp_f32_e32 v115, v115
	v_exp_f32_e32 v116, v116
	v_exp_f32_e32 v117, v117
	v_add_f32_e32 v114, 1.0, v114
	v_add_f32_e32 v115, 1.0, v115
	v_add_f32_e32 v116, 1.0, v116
	v_add_f32_e32 v117, 1.0, v117
	v_add_f32_e32 v104, v104, v248
	v_rcp_f32_e32 v114, v114
	v_add_f32_e32 v105, v105, v249
	v_rcp_f32_e32 v115, v115
	v_add_f32_e32 v106, v106, v250
	v_rcp_f32_e32 v116, v116
	v_add_f32_e32 v107, v107, v251
	v_rcp_f32_e32 v117, v117
	v_med3_f32 v104, v104, s53, v194
	v_med3_f32 v105, v105, s53, v194
	v_med3_f32 v106, v106, s53, v194
	v_med3_f32 v107, v107, s53, v194
	v_pk_add_f32 v[104:105], v[104:105], 1.0 op_sel_hi:[1,0]
	v_pk_add_f32 v[106:107], v[106:107], 1.0 op_sel_hi:[1,0]
	v_pk_mul_f32 v[104:105], v[108:109], v[104:105]
	v_pk_mul_f32 v[106:107], v[110:111], v[106:107]
	v_add_f32_e32 v100, v100, v244
	v_pk_mul_f32 v[108:109], v[104:105], v[114:115]
	v_pk_mul_f32 v[104:105], v[106:107], v[116:117]
	v_min_f32_e32 v100, 0x40e00000, v100
	v_cvt_pk_bf16_f32 v105, v104, v105
	v_mul_f32_e32 v104, 0x3fd9db23, v100
	v_add_f32_e32 v102, v102, v246
	v_add_f32_e32 v103, v103, v247
	v_mul_f32_e32 v104, 0xbfb8aa3b, v104
	v_add_f32_e32 v101, v101, v245
	v_min_f32_e32 v102, 0x40e00000, v102
	v_min_f32_e32 v103, 0x40e00000, v103
	v_exp_f32_e32 v106, v104
	v_cvt_pk_bf16_f32 v104, v108, v109
	v_min_f32_e32 v101, 0x40e00000, v101
	v_mul_f32_e32 v108, 0x3fd9db23, v102
	v_mul_f32_e32 v109, 0x3fd9db23, v103
	v_mul_f32_e32 v107, 0x3fd9db23, v101
	v_mul_f32_e32 v108, 0xbfb8aa3b, v108
	v_mul_f32_e32 v109, 0xbfb8aa3b, v109
	v_mul_f32_e32 v107, 0xbfb8aa3b, v107
	v_exp_f32_e32 v108, v108
	v_exp_f32_e32 v109, v109
	v_exp_f32_e32 v107, v107
	v_add_f32_e32 v106, 1.0, v106
	v_add_f32_e32 v108, 1.0, v108
	v_add_f32_e32 v109, 1.0, v109
	v_add_f32_e32 v107, 1.0, v107
	v_add_f32_e32 v98, v98, v240
	v_rcp_f32_e32 v108, v108
	v_add_f32_e32 v99, v99, v241
	v_rcp_f32_e32 v109, v109
	v_add_f32_e32 v96, v96, v238
	v_rcp_f32_e32 v106, v106
	v_add_f32_e32 v97, v97, v239
	v_rcp_f32_e32 v107, v107
	v_med3_f32 v98, v98, s53, v194
	v_med3_f32 v99, v99, s53, v194
	v_med3_f32 v96, v96, s53, v194
	v_med3_f32 v97, v97, s53, v194
	v_pk_add_f32 v[98:99], v[98:99], 1.0 op_sel_hi:[1,0]
	v_pk_add_f32 v[96:97], v[96:97], 1.0 op_sel_hi:[1,0]
	v_pk_mul_f32 v[98:99], v[102:103], v[98:99]
	v_add_f32_e32 v92, v92, v252
	v_add_f32_e32 v93, v93, v253
	v_add_f32_e32 v94, v94, v254
	v_add_f32_e32 v95, v95, v255
	v_pk_mul_f32 v[96:97], v[100:101], v[96:97]
	v_pk_mul_f32 v[98:99], v[98:99], v[108:109]
	v_min_f32_e32 v92, 0x40e00000, v92
	v_min_f32_e32 v93, 0x40e00000, v93
	v_min_f32_e32 v94, 0x40e00000, v94
	v_min_f32_e32 v95, 0x40e00000, v95
	v_pk_mul_f32 v[96:97], v[96:97], v[106:107]
	v_cvt_pk_bf16_f32 v107, v98, v99
	v_mul_f32_e32 v98, 0x3fd9db23, v92
	v_mul_f32_e32 v99, 0x3fd9db23, v93
	v_mul_f32_e32 v100, 0x3fd9db23, v94
	v_mul_f32_e32 v101, 0x3fd9db23, v95
	v_mul_f32_e32 v98, 0xbfb8aa3b, v98
	v_mul_f32_e32 v99, 0xbfb8aa3b, v99
	v_mul_f32_e32 v100, 0xbfb8aa3b, v100
	v_mul_f32_e32 v101, 0xbfb8aa3b, v101
	v_exp_f32_e32 v98, v98
	v_exp_f32_e32 v99, v99
	v_exp_f32_e32 v100, v100
	v_exp_f32_e32 v101, v101
	v_add_f32_e32 v98, 1.0, v98
	v_add_f32_e32 v99, 1.0, v99
	v_add_f32_e32 v100, 1.0, v100
	v_add_f32_e32 v101, 1.0, v101
	v_add_f32_e32 v88, v88, v248
	v_rcp_f32_e32 v98, v98
	v_add_f32_e32 v89, v89, v249
	v_rcp_f32_e32 v99, v99
	v_add_f32_e32 v90, v90, v250
	v_rcp_f32_e32 v100, v100
	v_add_f32_e32 v91, v91, v251
	v_rcp_f32_e32 v101, v101
	v_med3_f32 v88, v88, s53, v194
	v_med3_f32 v89, v89, s53, v194
	v_med3_f32 v90, v90, s53, v194
	v_med3_f32 v91, v91, s53, v194
	v_pk_add_f32 v[88:89], v[88:89], 1.0 op_sel_hi:[1,0]
	v_pk_add_f32 v[90:91], v[90:91], 1.0 op_sel_hi:[1,0]
	v_pk_mul_f32 v[88:89], v[92:93], v[88:89]
	v_pk_mul_f32 v[90:91], v[94:95], v[90:91]
	v_add_f32_e32 v80, v80, v244
	v_pk_mul_f32 v[92:93], v[88:89], v[98:99]
	v_pk_mul_f32 v[88:89], v[90:91], v[100:101]
	v_min_f32_e32 v80, 0x40e00000, v80
	v_cvt_pk_bf16_f32 v89, v88, v89
	v_mul_f32_e32 v88, 0x3fd9db23, v80
	v_add_f32_e32 v82, v82, v246
	v_add_f32_e32 v83, v83, v247
	v_mul_f32_e32 v88, 0xbfb8aa3b, v88
	v_add_f32_e32 v81, v81, v245
	v_min_f32_e32 v82, 0x40e00000, v82
	v_min_f32_e32 v83, 0x40e00000, v83
	v_exp_f32_e32 v90, v88
	v_cvt_pk_bf16_f32 v88, v92, v93
	v_min_f32_e32 v81, 0x40e00000, v81
	v_mul_f32_e32 v92, 0x3fd9db23, v82
	v_mul_f32_e32 v93, 0x3fd9db23, v83
	v_mul_f32_e32 v91, 0x3fd9db23, v81
	v_mul_f32_e32 v92, 0xbfb8aa3b, v92
	v_mul_f32_e32 v93, 0xbfb8aa3b, v93
	v_mul_f32_e32 v91, 0xbfb8aa3b, v91
	v_exp_f32_e32 v92, v92
	v_exp_f32_e32 v93, v93
	v_exp_f32_e32 v91, v91
	v_add3_u32 v180, s68, 16, v178
	v_ashrrev_i32_e32 v181, 31, v180
	v_lshlrev_b64 v[180:181], 12, v[180:181]
	v_add_f32_e32 v92, 1.0, v92
	v_add_f32_e32 v93, 1.0, v93
	v_lshl_add_u64 v[180:181], s[50:51], 0, v[180:181]
	v_add_f32_e32 v90, 1.0, v90
	v_add_f32_e32 v91, 1.0, v91
	v_add_f32_e32 v86, v86, v240
	v_rcp_f32_e32 v92, v92
	v_add_f32_e32 v87, v87, v241
	v_rcp_f32_e32 v93, v93
	v_cvt_pk_bf16_f32 v170, v160, v161
	v_lshl_add_u64 v[160:161], v[180:181], 0, v[176:177]
	v_add_f32_e32 v84, v84, v238
	v_rcp_f32_e32 v90, v90
	v_add_f32_e32 v85, v85, v239
	v_rcp_f32_e32 v91, v91
	v_med3_f32 v86, v86, s53, v194
	v_med3_f32 v87, v87, s53, v194
	global_store_dwordx4 v[160:161], v[168:171], off
	v_add3_u32 v160, s68, 32, v178
	v_med3_f32 v84, v84, s53, v194
	v_med3_f32 v85, v85, s53, v194
	v_pk_add_f32 v[86:87], v[86:87], 1.0 op_sel_hi:[1,0]
	v_ashrrev_i32_e32 v161, 31, v160
	v_pk_add_f32 v[84:85], v[84:85], 1.0 op_sel_hi:[1,0]
	v_pk_mul_f32 v[82:83], v[82:83], v[86:87]
	v_add_f32_e32 v76, v76, v252
	v_add_f32_e32 v77, v77, v253
	v_add_f32_e32 v78, v78, v254
	v_add_f32_e32 v79, v79, v255
	v_lshlrev_b64 v[160:161], 12, v[160:161]
	v_pk_mul_f32 v[80:81], v[80:81], v[84:85]
	v_pk_mul_f32 v[82:83], v[82:83], v[92:93]
	v_min_f32_e32 v76, 0x40e00000, v76
	v_min_f32_e32 v77, 0x40e00000, v77
	v_min_f32_e32 v78, 0x40e00000, v78
	v_min_f32_e32 v79, 0x40e00000, v79
	v_add_f32_e32 v52, v52, v252
	v_add_f32_e32 v36, v36, v244
	v_lshl_add_u64 v[160:161], s[50:51], 0, v[160:161]
	v_pk_mul_f32 v[80:81], v[80:81], v[90:91]
	v_cvt_pk_bf16_f32 v91, v82, v83
	v_mul_f32_e32 v82, 0x3fd9db23, v76
	v_mul_f32_e32 v83, 0x3fd9db23, v77
	v_mul_f32_e32 v84, 0x3fd9db23, v78
	v_mul_f32_e32 v85, 0x3fd9db23, v79
	v_min_f32_e32 v52, 0x40e00000, v52
	v_min_f32_e32 v36, 0x40e00000, v36
	v_cvt_pk_bf16_f32 v154, v144, v145
	v_lshl_add_u64 v[144:145], v[160:161], 0, v[176:177]
	v_mul_f32_e32 v82, 0xbfb8aa3b, v82
	v_mul_f32_e32 v83, 0xbfb8aa3b, v83
	v_mul_f32_e32 v84, 0xbfb8aa3b, v84
	v_mul_f32_e32 v85, 0xbfb8aa3b, v85
	v_add_f32_e32 v68, v68, v244
	v_mul_f32_e32 v60, 0x3fd9db23, v52
	v_mul_f32_e32 v44, 0x3fd9db23, v36
	global_store_dwordx4 v[144:145], v[152:155], off
	v_add3_u32 v144, s68, 48, v178
	v_exp_f32_e32 v82, v82
	v_exp_f32_e32 v83, v83
	v_exp_f32_e32 v84, v84
	v_exp_f32_e32 v85, v85
	v_mul_f32_e32 v60, 0xbfb8aa3b, v60
	v_mul_f32_e32 v44, 0xbfb8aa3b, v44
	v_ashrrev_i32_e32 v145, 31, v144
	v_exp_f32_e32 v60, v60
	v_exp_f32_e32 v44, v44
	v_lshlrev_b64 v[144:145], 12, v[144:145]
	v_lshl_add_u64 v[144:145], s[50:51], 0, v[144:145]
	v_add_f32_e32 v53, v53, v253
	v_add_f32_e32 v37, v37, v245
	v_cvt_pk_bf16_f32 v138, v128, v129
	v_lshl_add_u64 v[128:129], v[144:145], 0, v[176:177]
	v_add_f32_e32 v82, 1.0, v82
	v_add_f32_e32 v83, 1.0, v83
	v_add_f32_e32 v84, 1.0, v84
	v_add_f32_e32 v85, 1.0, v85
	v_min_f32_e32 v53, 0x40e00000, v53
	v_min_f32_e32 v37, 0x40e00000, v37
	global_store_dwordx4 v[128:129], v[136:139], off
	v_add3_u32 v128, s68, 64, v178
	v_add_f32_e32 v72, v72, v248
	v_rcp_f32_e32 v82, v82
	v_add_f32_e32 v73, v73, v249
	v_rcp_f32_e32 v83, v83
	v_add_f32_e32 v74, v74, v250
	v_rcp_f32_e32 v84, v84
	v_add_f32_e32 v75, v75, v251
	v_rcp_f32_e32 v85, v85
	v_add_f32_e32 v64, v64, v238
	v_add_f32_e32 v48, v48, v248
	v_add_f32_e32 v56, 1.0, v60
	v_mul_f32_e32 v60, 0x3fd9db23, v53
	v_add_f32_e32 v32, v32, v238
	v_add_f32_e32 v40, 1.0, v44
	v_mul_f32_e32 v44, 0x3fd9db23, v37
	v_ashrrev_i32_e32 v129, 31, v128
	v_med3_f32 v72, v72, s53, v194
	v_med3_f32 v73, v73, s53, v194
	v_med3_f32 v74, v74, s53, v194
	v_med3_f32 v75, v75, s53, v194
	v_mul_f32_e32 v60, 0xbfb8aa3b, v60
	v_mul_f32_e32 v44, 0xbfb8aa3b, v44
	v_lshlrev_b64 v[128:129], 12, v[128:129]
	v_pk_add_f32 v[72:73], v[72:73], 1.0 op_sel_hi:[1,0]
	v_pk_add_f32 v[74:75], v[74:75], 1.0 op_sel_hi:[1,0]
	v_exp_f32_e32 v60, v60
	v_exp_f32_e32 v44, v44
	v_lshl_add_u64 v[128:129], s[50:51], 0, v[128:129]
	v_pk_mul_f32 v[74:75], v[78:79], v[74:75]
	v_pk_mul_f32 v[72:73], v[76:77], v[72:73]
	v_cvt_pk_bf16_f32 v122, v112, v113
	v_lshl_add_u64 v[112:113], v[128:129], 0, v[176:177]
	v_pk_mul_f32 v[76:77], v[72:73], v[82:83]
	v_pk_mul_f32 v[72:73], v[74:75], v[84:85]
	v_min_f32_e32 v68, 0x40e00000, v68
	v_add_f32_e32 v54, v54, v254
	v_add_f32_e32 v38, v38, v246
	global_store_dwordx4 v[112:113], v[120:123], off
	v_add_u32_e32 v112, s16, v178
	v_cvt_pk_bf16_f32 v73, v72, v73
	v_mul_f32_e32 v72, 0x3fd9db23, v68
	v_add_f32_e32 v69, v69, v245
	v_add_f32_e32 v70, v70, v246
	v_add_f32_e32 v71, v71, v247
	v_min_f32_e32 v54, 0x40e00000, v54
	v_min_f32_e32 v38, 0x40e00000, v38
	v_ashrrev_i32_e32 v113, 31, v112
	v_mul_f32_e32 v72, 0xbfb8aa3b, v72
	v_min_f32_e32 v69, 0x40e00000, v69
	v_add_f32_e32 v65, v65, v239
	v_min_f32_e32 v70, 0x40e00000, v70
	v_min_f32_e32 v71, 0x40e00000, v71
	v_add_f32_e32 v49, v49, v249
	v_add_f32_e32 v57, 1.0, v60
	v_mul_f32_e32 v60, 0x3fd9db23, v54
	v_add_f32_e32 v33, v33, v239
	v_add_f32_e32 v41, 1.0, v44
	v_mul_f32_e32 v44, 0x3fd9db23, v38
	v_lshlrev_b64 v[112:113], 12, v[112:113]
	v_exp_f32_e32 v74, v72
	v_cvt_pk_bf16_f32 v72, v76, v77
	v_mul_f32_e32 v75, 0x3fd9db23, v69
	v_mul_f32_e32 v76, 0x3fd9db23, v70
	v_mul_f32_e32 v77, 0x3fd9db23, v71
	v_mul_f32_e32 v60, 0xbfb8aa3b, v60
	v_mul_f32_e32 v44, 0xbfb8aa3b, v44
	v_lshl_add_u64 v[112:113], s[50:51], 0, v[112:113]
	v_mul_f32_e32 v75, 0xbfb8aa3b, v75
	v_mul_f32_e32 v76, 0xbfb8aa3b, v76
	v_mul_f32_e32 v77, 0xbfb8aa3b, v77
	v_exp_f32_e32 v60, v60
	v_exp_f32_e32 v44, v44
	v_cvt_pk_bf16_f32 v106, v96, v97
	v_lshl_add_u64 v[96:97], v[112:113], 0, v[176:177]
	s_add_i32 s16, s68, 0x60
	v_exp_f32_e32 v75, v75
	v_exp_f32_e32 v76, v76
	v_exp_f32_e32 v77, v77
	global_store_dwordx4 v[96:97], v[104:107], off
	v_add_u32_e32 v96, s16, v178
	v_add_f32_e32 v55, v55, v255
	v_add_f32_e32 v39, v39, v247
	v_ashrrev_i32_e32 v97, 31, v96
	v_min_f32_e32 v55, 0x40e00000, v55
	v_min_f32_e32 v39, 0x40e00000, v39
	v_lshlrev_b64 v[96:97], 12, v[96:97]
	v_add_f32_e32 v66, v66, v240
	v_add_f32_e32 v50, v50, v250
	v_add_f32_e32 v58, 1.0, v60
	v_mul_f32_e32 v60, 0x3fd9db23, v55
	v_add_f32_e32 v34, v34, v240
	v_add_f32_e32 v42, 1.0, v44
	v_mul_f32_e32 v44, 0x3fd9db23, v39
	v_lshl_add_u64 v[96:97], s[50:51], 0, v[96:97]
	v_add_f32_e32 v74, 1.0, v74
	v_add_f32_e32 v75, 1.0, v75
	v_add_f32_e32 v76, 1.0, v76
	v_add_f32_e32 v77, 1.0, v77
	v_mul_f32_e32 v60, 0xbfb8aa3b, v60
	v_mul_f32_e32 v44, 0xbfb8aa3b, v44
	v_cvt_pk_bf16_f32 v90, v80, v81
	v_lshl_add_u64 v[80:81], v[96:97], 0, v[176:177]
	s_add_i32 s16, s68, 0x70
	v_rcp_f32_e32 v74, v74
	v_rcp_f32_e32 v75, v75
	v_rcp_f32_e32 v76, v76
	v_add_f32_e32 v67, v67, v241
	v_rcp_f32_e32 v77, v77
	v_exp_f32_e32 v60, v60
	v_exp_f32_e32 v44, v44
	global_store_dwordx4 v[80:81], v[88:91], off
	v_add_u32_e32 v80, s16, v178
	v_med3_f32 v64, v64, s53, v194
	v_med3_f32 v65, v65, s53, v194
	v_med3_f32 v66, v66, s53, v194
	v_med3_f32 v67, v67, s53, v194
	v_ashrrev_i32_e32 v81, 31, v80
	v_pk_add_f32 v[64:65], v[64:65], 1.0 op_sel_hi:[1,0]
	v_pk_add_f32 v[66:67], v[66:67], 1.0 op_sel_hi:[1,0]
	v_lshlrev_b64 v[80:81], 12, v[80:81]
	v_pk_mul_f32 v[66:67], v[70:71], v[66:67]
	v_pk_mul_f32 v[64:65], v[68:69], v[64:65]
	v_lshl_add_u64 v[80:81], s[50:51], 0, v[80:81]
	v_pk_mul_f32 v[64:65], v[64:65], v[74:75]
	v_pk_mul_f32 v[66:67], v[66:67], v[76:77]
	v_add_f32_e32 v51, v51, v251
	v_add_f32_e32 v59, 1.0, v60
	v_add_f32_e32 v35, v35, v241
	v_add_f32_e32 v43, 1.0, v44
	v_cvt_pk_bf16_f32 v75, v66, v67
	v_cvt_pk_bf16_f32 v74, v64, v65
	v_lshl_add_u64 v[64:65], v[80:81], 0, v[176:177]
	s_add_i32 s16, s68, 0x80
	v_rcp_f32_e32 v56, v56
	v_rcp_f32_e32 v57, v57
	v_rcp_f32_e32 v58, v58
	v_rcp_f32_e32 v59, v59
	v_rcp_f32_e32 v40, v40
	v_rcp_f32_e32 v41, v41
	v_rcp_f32_e32 v42, v42
	v_rcp_f32_e32 v43, v43
	global_store_dwordx4 v[64:65], v[72:75], off
	v_add_u32_e32 v64, s16, v178
	v_med3_f32 v48, v48, s53, v194
	v_med3_f32 v49, v49, s53, v194
	v_med3_f32 v50, v50, s53, v194
	v_med3_f32 v51, v51, s53, v194
	v_med3_f32 v32, v32, s53, v194
	v_med3_f32 v33, v33, s53, v194
	v_med3_f32 v34, v34, s53, v194
	v_med3_f32 v35, v35, s53, v194
	v_ashrrev_i32_e32 v65, 31, v64
	v_pk_add_f32 v[48:49], v[48:49], 1.0 op_sel_hi:[1,0]
	v_pk_add_f32 v[50:51], v[50:51], 1.0 op_sel_hi:[1,0]
	v_pk_add_f32 v[32:33], v[32:33], 1.0 op_sel_hi:[1,0]
	v_pk_add_f32 v[34:35], v[34:35], 1.0 op_sel_hi:[1,0]
	v_lshlrev_b64 v[64:65], 12, v[64:65]
	v_pk_mul_f32 v[50:51], v[54:55], v[50:51]
	v_pk_mul_f32 v[48:49], v[52:53], v[48:49]
	v_pk_mul_f32 v[34:35], v[38:39], v[34:35]
	v_pk_mul_f32 v[32:33], v[36:37], v[32:33]
	v_lshl_add_u64 v[64:65], s[50:51], 0, v[64:65]
	v_pk_mul_f32 v[52:53], v[48:49], v[56:57]
	v_pk_mul_f32 v[48:49], v[50:51], v[58:59]
	v_pk_mul_f32 v[32:33], v[32:33], v[40:41]
	v_pk_mul_f32 v[34:35], v[34:35], v[42:43]
	v_cvt_pk_bf16_f32 v49, v48, v49
	v_cvt_pk_bf16_f32 v48, v52, v53
	v_cvt_pk_bf16_f32 v51, v34, v35
	v_cvt_pk_bf16_f32 v50, v32, v33
	v_lshl_add_u64 v[32:33], v[64:65], 0, v[176:177]
	s_mov_b32 s68, s43
	global_store_dwordx4 v[32:33], v[48:51], off
	s_cbranch_vccnz .LBB0_663
